# speedup vs baseline: 1.0389x; 1.0101x over previous
.Lrec_loop:
	s_add_i32 s10, s36, -1
	s_and_b32 s54, s10, 1
	v_lshl_add_u32 v164, s54, 18, v186
	s_bfe_u32 s54, s10, 0x10001
	s_mul_i32 s54, s54, 0x40004000
	s_sleep 10
	buffer_load_dwordx4 v[16:19], v164, s[16:19], 0 offen sc1
	buffer_load_dwordx4 v[20:23], v164, s[16:19], 0 offen offset:1024 sc1
	buffer_load_dwordx4 v[24:27], v164, s[16:19], 0 offen offset:2048 sc1
	buffer_load_dwordx4 v[28:31], v164, s[16:19], 0 offen offset:3072 sc1
	s_lshl_b32 s41, s36, 7
	s_mov_b32 s43, 0
	s_mov_b32 s45, 15
	s_mov_b32 s46, 0
	s_mov_b32 s55, 0
	s_add_i32 s11, s41, 0x80
	v_add_u32_e32 v206, s11, v169
	v_mov_b32_e32 v207, 0
	v_lshlrev_b64 v[206:207], 14, v[206:207]
	v_lshl_add_u64 v[206:207], v[174:175], 0, v[206:207]
	s_lshl_b32 s11, s36, 16
	s_and_b32 s11, s11, 0x10000
	v_add_u32_e32 v173, s11, v170
	s_waitcnt vmcnt(3)
	v_xor_b32_e32 v16, s54, v16
	v_xor_b32_e32 v17, s54, v17
	v_xor_b32_e32 v18, s54, v18
	v_xor_b32_e32 v19, s54, v19
	v_or3_b32 v0, v16, v17, v18
	v_bitop3_b32 v0, v0, s39, v19 bitop3:0xc8
	v_cmp_ne_u32_e32 vcc, 0, v0
	s_cmp_lg_u64 vcc, 0
	s_cbranch_scc1 .Lrec_e0dirty
	s_bitset0_b32 s45, 0
	v_mfma_f32_16x16x32_f16 v[198:201], v[152:155], v[16:19], 0
	v_mfma_f32_16x16x32_f16 v[202:205], v[48:51], v[16:19], 0
	v_mfma_f32_16x16x32_f16 v[212:215], v[88:91], v[16:19], 0
	v_mfma_f32_16x16x32_f16 v[216:219], v[92:95], v[16:19], 0
	v_mfma_f32_16x16x32_f16 v[220:223], v[108:111], v[16:19], 0
	v_mfma_f32_16x16x32_f16 v[224:227], v[112:115], v[16:19], 0
	v_mfma_f32_16x16x32_f16 v[228:231], v[140:143], v[16:19], 0
	v_mfma_f32_16x16x32_f16 v[232:235], v[32:35], v[16:19], v[160:163]
	s_mov_b32 s46, 1
	s_branch .Lrec_wait
.Lrec_e0dirty:
	buffer_load_dwordx4 v[16:19], v164, s[16:19], 0 offen sc1
.Lrec_wait:
	s_waitcnt vmcnt(0)

	.amdhsa_kernel _Z15lstm_persistentPKDF16_PKfPDF16_PjS4_S2_S3_
		.amdhsa_group_segment_fixed_size 0
		.amdhsa_private_segment_fixed_size 0
		.amdhsa_kernarg_size 56
		.amdhsa_user_sgpr_count 2
		.amdhsa_user_sgpr_dispatch_ptr 0
		.amdhsa_user_sgpr_queue_ptr 0
		.amdhsa_user_sgpr_kernarg_segment_ptr 1
		.amdhsa_user_sgpr_dispatch_id 0
		.amdhsa_user_sgpr_kernarg_preload_length 0
		.amdhsa_user_sgpr_kernarg_preload_offset 0
		.amdhsa_user_sgpr_private_segment_size 0
		.amdhsa_uses_dynamic_stack 0
		.amdhsa_enable_private_segment 0
		.amdhsa_system_sgpr_workgroup_id_x 1
		.amdhsa_system_sgpr_workgroup_id_y 0
		.amdhsa_system_sgpr_workgroup_id_z 0
		.amdhsa_system_sgpr_workgroup_info 0
		.amdhsa_system_vgpr_workitem_id 0
		.amdhsa_next_free_vgpr 246
		.amdhsa_next_free_sgpr 56
		.amdhsa_accum_offset 248
		.amdhsa_reserve_vcc 1
		.amdhsa_float_round_mode_32 0
		.amdhsa_float_round_mode_16_64 0
		.amdhsa_float_denorm_mode_32 3
		.amdhsa_float_denorm_mode_16_64 3
		.amdhsa_dx10_clamp 1
		.amdhsa_ieee_mode 1
		.amdhsa_fp16_overflow 0
		.amdhsa_tg_split 0
		.amdhsa_exception_fp_ieee_invalid_op 0
		.amdhsa_exception_fp_denorm_src 0
		.amdhsa_exception_fp_ieee_div_zero 0
		.amdhsa_exception_fp_ieee_overflow 0
		.amdhsa_exception_fp_ieee_underflow 0
		.amdhsa_exception_fp_ieee_inexact 0
		.amdhsa_exception_int_div_zero 0
	.end_amdhsa_kernel

amdhsa.kernels:
  - .agpr_count:     0
    .args:
      - .actual_access:  read_only
        .address_space:  global
        .offset:         0
        .size:           8
        .value_kind:     global_buffer
      - .actual_access:  read_only
        .address_space:  global
        .offset:         8
        .size:           8
        .value_kind:     global_buffer
      - .actual_access:  read_only
        .address_space:  global
        .offset:         16
        .size:           8
        .value_kind:     global_buffer
      - .actual_access:  read_only
        .address_space:  global
        .offset:         24
        .size:           8
        .value_kind:     global_buffer
      - .actual_access:  read_only
        .address_space:  global
        .offset:         32
        .size:           8
        .value_kind:     global_buffer
      - .actual_access:  read_only
        .address_space:  global
        .offset:         40
        .size:           8
        .value_kind:     global_buffer
      - .address_space:  global
        .offset:         48
        .size:           8
        .value_kind:     global_buffer
      - .address_space:  global
        .offset:         56
        .size:           8
        .value_kind:     global_buffer
      - .address_space:  global
        .offset:         64
        .size:           8
        .value_kind:     global_buffer
      - .address_space:  global
        .offset:         72
        .size:           8
        .value_kind:     global_buffer
      - .address_space:  global
        .offset:         80
        .size:           8
        .value_kind:     global_buffer
    .group_segment_fixed_size: 0
    .kernarg_segment_align: 8
    .kernarg_segment_size: 88
    .language:       OpenCL C
    .language_version:
      - 2
      - 0
    .max_flat_workgroup_size: 256
    .name:           _Z11prep_kernelPKfPKiS0_S0_S0_S0_PDF16_S3_S3_S3_Pc
    .private_segment_fixed_size: 0
    .sgpr_count:     33
    .sgpr_spill_count: 0
    .symbol:         _Z11prep_kernelPKfPKiS0_S0_S0_S0_PDF16_S3_S3_S3_Pc.kd
    .uniform_work_group_size: 1
    .uses_dynamic_stack: false
    .vgpr_count:     14
    .vgpr_spill_count: 0
    .wavefront_size: 64
  - .agpr_count:     0
    .args:
      - .actual_access:  read_only
        .address_space:  global
        .offset:         0
        .size:           8
        .value_kind:     global_buffer
      - .address_space:  global
        .offset:         8
        .size:           8
        .value_kind:     global_buffer
    .group_segment_fixed_size: 0
    .kernarg_segment_align: 8
    .kernarg_segment_size: 16
    .language:       OpenCL C
    .language_version:
      - 2
      - 0
    .max_flat_workgroup_size: 256
    .name:           _Z7cvt_wfcPKfPDF16_
    .private_segment_fixed_size: 0
    .sgpr_count:     12
    .sgpr_spill_count: 0
    .symbol:         _Z7cvt_wfcPKfPDF16_.kd
    .uniform_work_group_size: 1
    .uses_dynamic_stack: false
    .vgpr_count:     12
    .vgpr_spill_count: 0
    .wavefront_size: 64
  - .agpr_count:     12
    .args:
      - .actual_access:  read_only
        .address_space:  global
        .offset:         0
        .size:           8
        .value_kind:     global_buffer
      - .actual_access:  read_only
        .address_space:  global
        .offset:         8
        .size:           8
        .value_kind:     global_buffer
      - .address_space:  global
        .offset:         16
        .size:           8
        .value_kind:     global_buffer
      - .address_space:  global
        .offset:         24
        .size:           8
        .value_kind:     global_buffer
      - .offset:         32
        .size:           4
        .value_kind:     by_value
    .group_segment_fixed_size: 0
    .kernarg_segment_align: 8
    .kernarg_segment_size: 36
    .language:       OpenCL C
    .language_version:
      - 2
      - 0
    .max_flat_workgroup_size: 256
    .name:           _Z9lstm_stepPKfS0_PDF16_Pfi
    .private_segment_fixed_size: 0
    .sgpr_count:     21
    .sgpr_spill_count: 0
    .symbol:         _Z9lstm_stepPKfS0_PDF16_Pfi.kd
    .uniform_work_group_size: 1
    .uses_dynamic_stack: false
    .vgpr_count:     88
    .vgpr_spill_count: 0
    .wavefront_size: 64
  - .agpr_count:     0
    .args:
      - .actual_access:  read_only
        .address_space:  global
        .offset:         0
        .size:           8
        .value_kind:     global_buffer
      - .actual_access:  read_only
        .address_space:  global
        .offset:         8
        .size:           8
        .value_kind:     global_buffer
      - .address_space:  global
        .offset:         16
        .size:           8
        .value_kind:     global_buffer
      - .address_space:  global
        .offset:         24
        .size:           8
        .value_kind:     global_buffer
      - .address_space:  global
        .offset:         32
        .size:           8
        .value_kind:     global_buffer
      - .actual_access:  read_only
        .address_space:  global
        .offset:         40
        .size:           8
        .value_kind:     global_buffer
      - .address_space:  global
        .offset:         48
        .size:           8
        .value_kind:     global_buffer
    .group_segment_fixed_size: 0
    .kernarg_segment_align: 8
    .kernarg_segment_size: 56
    .language:       OpenCL C
    .language_version:
      - 2
      - 0
    .max_flat_workgroup_size: 512
    .name:           _Z15lstm_persistentPKDF16_PKfPDF16_PjS4_S2_S3_
    .private_segment_fixed_size: 0
    .sgpr_count:     62
    .sgpr_spill_count: 0
    .symbol:         _Z15lstm_persistentPKDF16_PKfPDF16_PjS4_S2_S3_.kd
    .uniform_work_group_size: 1
    .uses_dynamic_stack: false
    .vgpr_count:     246
    .vgpr_spill_count: 0
    .wavefront_size: 64
  - .agpr_count:     0
    .args:
      - .address_space:  global
        .offset:         0
        .size:           8
        .value_kind:     global_buffer
      - .address_space:  global
        .offset:         8
        .size:           8
        .value_kind:     global_buffer
      - .address_space:  global
        .offset:         16
        .size:           8
        .value_kind:     global_buffer
      - .address_space:  global
        .offset:         24
        .size:           8
        .value_kind:     global_buffer
      - .address_space:  global
        .offset:         32
        .size:           8
        .value_kind:     global_buffer
      - .offset:         40
        .size:           4
        .value_kind:     hidden_block_count_x
      - .offset:         44
        .size:           4
        .value_kind:     hidden_block_count_y
      - .offset:         48
        .size:           4
        .value_kind:     hidden_block_count_z
      - .offset:         52
        .size:           2
        .value_kind:     hidden_group_size_x
      - .offset:         54
        .size:           2
        .value_kind:     hidden_group_size_y
      - .offset:         56
        .size:           2
        .value_kind:     hidden_group_size_z
      - .offset:         58
        .size:           2
        .value_kind:     hidden_remainder_x
      - .offset:         60
        .size:           2
        .value_kind:     hidden_remainder_y
      - .offset:         62
        .size:           2
        .value_kind:     hidden_remainder_z
      - .offset:         80
        .size:           8
        .value_kind:     hidden_global_offset_x
      - .offset:         88
        .size:           8
        .value_kind:     hidden_global_offset_y
      - .offset:         96
        .size:           8
        .value_kind:     hidden_global_offset_z
      - .offset:         104
        .size:           2
        .value_kind:     hidden_grid_dims
      - .offset:         160
        .size:           4
        .value_kind:     hidden_dynamic_lds_size
    .group_segment_fixed_size: 0
    .kernarg_segment_align: 8
    .kernarg_segment_size: 296
    .language:       OpenCL C
    .language_version:
      - 2
      - 0
    .max_flat_workgroup_size: 512
    .name:           _Z11gemm_8phaseILi0EEvPKDF16_S1_PfPKfS4_
    .private_segment_fixed_size: 0
    .sgpr_count:     59
    .sgpr_spill_count: 0
    .symbol:         _Z11gemm_8phaseILi0EEvPKDF16_S1_PfPKfS4_.kd
    .uniform_work_group_size: 1
    .uses_dynamic_stack: false
    .vgpr_count:     250
    .vgpr_spill_count: 0
    .wavefront_size: 64
  - .agpr_count:     0
    .args:
      - .address_space:  global
        .offset:         0
        .size:           8
        .value_kind:     global_buffer
      - .address_space:  global
        .offset:         8
        .size:           8
        .value_kind:     global_buffer
      - .address_space:  global
        .offset:         16
        .size:           8
        .value_kind:     global_buffer
      - .address_space:  global
        .offset:         24
        .size:           8
        .value_kind:     global_buffer
      - .address_space:  global
        .offset:         32
        .size:           8
        .value_kind:     global_buffer
      - .offset:         40
        .size:           4
        .value_kind:     hidden_block_count_x
      - .offset:         44
        .size:           4
        .value_kind:     hidden_block_count_y
      - .offset:         48
        .size:           4
        .value_kind:     hidden_block_count_z
      - .offset:         52
        .size:           2
        .value_kind:     hidden_group_size_x
      - .offset:         54
        .size:           2
        .value_kind:     hidden_group_size_y
      - .offset:         56
        .size:           2
        .value_kind:     hidden_group_size_z
      - .offset:         58
        .size:           2
        .value_kind:     hidden_remainder_x
      - .offset:         60
        .size:           2
        .value_kind:     hidden_remainder_y
      - .offset:         62
        .size:           2
        .value_kind:     hidden_remainder_z
      - .offset:         80
        .size:           8
        .value_kind:     hidden_global_offset_x
      - .offset:         88
        .size:           8
        .value_kind:     hidden_global_offset_y
      - .offset:         96
        .size:           8
        .value_kind:     hidden_global_offset_z
      - .offset:         104
        .size:           2
        .value_kind:     hidden_grid_dims
      - .offset:         160
        .size:           4
        .value_kind:     hidden_dynamic_lds_size
    .group_segment_fixed_size: 0
    .kernarg_segment_align: 8
    .kernarg_segment_size: 296
    .language:       OpenCL C
    .language_version:
      - 2
      - 0
    .max_flat_workgroup_size: 512
    .name:           _Z11gemm_8phaseILi1EEvPKDF16_S1_PfPKfS4_
    .private_segment_fixed_size: 0
    .sgpr_count:     44
    .sgpr_spill_count: 0
    .symbol:         _Z11gemm_8phaseILi1EEvPKDF16_S1_PfPKfS4_.kd
    .uniform_work_group_size: 1
    .uses_dynamic_stack: false
    .vgpr_count:     256
    .vgpr_spill_count: 0
    .wavefront_size: 64
